# speedup vs baseline: 1.0028x; 1.0028x over previous
.Lskip_stage0:
	s_ashr_i32 s2, s4, 6
	s_lshl_b32 s3, s2, 3
	s_and_b32 s5, s3, 8
	s_bfe_u32 s26, s2, 0x10001
	s_or_b32 s5, s26, s5
	s_lshl_b32 s26, s2, 9
	s_and_b32 s26, s26, 0x400
	s_lshl_b32 s5, s5, 4
	s_or_b32 s28, s5, s26
	v_lshrrev_b32_e32 v182, 5, v167
	v_bfe_u32 v2, v156, 4, 1
	v_bitop3_b32 v3, v182, v156, 1 bitop3:0x78
	v_lshlrev_b32_e32 v154, 2, v182
	v_xor_b32_e32 v3, v3, v2
	v_bitop3_b32 v4, v154, v156, 4 bitop3:0x78
	v_and_b32_e32 v5, 10, v156
	v_or3_b32 v3, v5, v4, v3
	s_lshl_b32 s5, s2, 4
	v_lshlrev_b32_e32 v3, 4, v3
	s_lshl_b32 s3, s2, 13
	s_and_b32 s29, s5, 16
	v_lshlrev_b32_e32 v170, 8, v182
	v_lshl_or_b32 v171, v2, 10, v3
	s_or_b32 s26, s29, s3
	v_bitop3_b32 v179, v171, s26, v170 bitop3:0x36
	s_or_b32 s5, s26, 0x280
	v_bitop3_b32 v178, v171, s5, v170 bitop3:0x36
	s_or_b32 s30, s3, 0x800
	s_or_b32 s33, s3, 0x1000
	s_or_b32 s29, s29, 64
	s_or_b32 s34, s29, s33
	v_bitop3_b32 v180, v171, s34, v170 bitop3:0x36
	s_or_b32 s29, s3, s29
	s_or_b32 s29, s29, 0x1280
	s_and_b32 s5, s2, 1
	s_lshl_b32 s31, s5, 4
	s_or_b32 s2, s31, s3
	v_bitop3_b32 v173, v171, s2, v170 bitop3:0x36
	v_bitop3_b32 v34, v156, 31, v156 bitop3:0xc
	v_lshrrev_b32_e32 v35, 4, v34
	v_bitop3_b32 v36, v34, v182, 1 bitop3:0x6c
	v_xor_b32_e32 v36, v36, v35
	v_bitop3_b32 v34, v34, v154, 4 bitop3:0x6c
	v_bitop3_b32 v37, v156, 10, 31 bitop3:8
	v_or3_b32 v34, v37, v34, v36
	v_lshlrev_b32_e32 v35, 10, v35
	v_lshlrev_b32_e32 v34, 4, v34
	v_or3_b32 v154, v35, v34, v170
	v_bitop3_b32 v172, s2, v154, v159 bitop3:0x36
	v_bitop3_b32 v176, v171, s29, v170 bitop3:0x36
	s_or_b32 s29, s31, s30
	s_or_b32 s29, s29, 0xa0
	v_bitop3_b32 v175, v171, s29, v170 bitop3:0x36
	s_or_b32 s29, s2, 0xaa0
	s_xor_b32 s29, s29, 0x80
	v_xor_b32_e32 v174, s29, v154
	s_or_b32 s29, s26, 0x18e0
	v_bitop3_b32 v181, v171, s29, v170 bitop3:0x36
	s_or_b32 s29, s26, 0x1a60
	v_bitop3_b32 v177, v171, s29, v170 bitop3:0x36
	s_or_b32 s29, s31, 64
	s_or_b32 s3, s3, s29
	s_mov_b32 s41, s3
	s_or_b32 s29, s29, s33
	s_mov_b32 s40, s29
	s_or_b32 s3, s2, 0x18e0
	s_mov_b32 s42, s3
	s_or_b32 s2, s2, 0x1ae0
	s_xor_b32 s2, s2, 0x80
	s_mov_b32 s43, s2
	s_lshr_b32 s38, s4, 1
	v_and_b32_e32 v26, 31, v167
	v_and_b32_e32 v27, 3, v167
	v_bfe_u32 v28, v167, 3, 1
	v_bfe_u32 v29, v167, 2, 1
	v_lshl_or_b32 v27, v28, 2, v27
	v_lshl_or_b32 v27, v29, 3, v27
	v_lshlrev_b32_e32 v32, 9, v182
	v_lshl_add_u32 v30, v27, 3, v32
	v_add_u32_e32 v30, 0x10000, v30
	v_lshl_add_u32 v31, v26, 3, v32
	v_add_u32_e32 v31, 0x10400, v31
	v_xor_b32_e32 v28, 31, v26
	v_lshl_add_u32 v28, v28, 3, v32
	v_add_u32_e32 v28, 0x10400, v28
	v_bfe_u32 v29, v167, 4, 1
	v_mul_u32_u24_e32 v29, 0x78, v29
	v_xor_b32_e32 v254, s38, v29
	v_or_b32_e32 v254, 0x10800, v254
	v_and_b32_e32 v33, 16, v167
	v_cmp_eq_u32_e32 vcc, 0, v33
	ds_read2_b64 v[66:69], v30 offset0:0 offset1:32
	ds_read2_b64 v[70:73], v30 offset0:16 offset1:48
	ds_read2_b64 v[198:201], v31 offset0:0 offset1:32
	ds_read2_b64 v[202:205], v28 offset0:0 offset1:32
	ds_read2_b64 v[206:209], v254 offset0:0 offset1:16
	ds_read2_b64 v[210:213], v254 offset0:32 offset1:48
	s_waitcnt lgkmcnt(0)
	v_cndmask_b32_e32 v74, v67, v66, vcc
	v_cndmask_b32_e32 v75, v69, v68, vcc
	v_cndmask_b32_e64 v76, v66, -v67, vcc
	v_cndmask_b32_e64 v77, v68, -v69, vcc
	v_cndmask_b32_e32 v78, v71, v70, vcc
	v_cndmask_b32_e32 v79, v73, v72, vcc
	v_cndmask_b32_e64 v80, v70, -v71, vcc
	v_cndmask_b32_e64 v81, v72, -v73, vcc
	v_cvt_pk_f16_f32 v190, v74, v75
	v_cvt_pk_f16_f32 v191, v74, v75
	v_cvt_pk_f16_f32 v192, v76, v77
	v_cvt_pk_f16_f32 v193, v76, v77
	v_cvt_pk_f16_f32 v194, v78, v79
	v_cvt_pk_f16_f32 v195, v78, v79
	v_cvt_pk_f16_f32 v196, v80, v81
	v_cvt_pk_f16_f32 v197, v80, v81
	v_mul_f32_e32 v66, v199, v207
	v_mul_f32_e32 v68, v199, v206
	v_mul_f32_e32 v67, v199, v209
	v_mul_f32_e32 v69, v199, v208
	v_fma_f32 v66, v198, v206, -v66
	v_fma_f32 v68, v198, v207, v68
	v_fma_f32 v67, v198, v208, -v67
	v_fma_f32 v69, v198, v209, v69
	v_cvt_pk_f16_f32 v214, v66, v67
	v_cvt_pk_f16_f32 v216, v68, v69
	v_mul_f32_e32 v70, v201, v211
	v_mul_f32_e32 v72, v201, v210
	v_mul_f32_e32 v71, v201, v213
	v_mul_f32_e32 v73, v201, v212
	v_fma_f32 v70, v200, v210, -v70
	v_fma_f32 v72, v200, v211, v72
	v_fma_f32 v71, v200, v212, -v71
	v_fma_f32 v73, v200, v213, v73
	v_cvt_pk_f16_f32 v215, v70, v71
	v_cvt_pk_f16_f32 v217, v72, v73
	v_mul_f32_e32 v66, v203, v207
	v_mul_f32_e32 v68, v203, v206
	v_mul_f32_e32 v67, v203, v209
	v_mul_f32_e32 v69, v203, v208
	v_fma_f32 v66, v202, v206, -v66
	v_fma_f32 v68, v202, v207, v68
	v_fma_f32 v67, v202, v208, -v67
	v_fma_f32 v69, v202, v209, v69
	v_cvt_pk_f16_f32 v218, v66, v67
	v_cvt_pk_f16_f32 v220, v68, v69
	v_mul_f32_e32 v70, v205, v211
	v_mul_f32_e32 v72, v205, v210
	v_mul_f32_e32 v71, v205, v213
	v_mul_f32_e32 v73, v205, v212
	v_fma_f32 v70, v204, v210, -v70
	v_fma_f32 v72, v204, v211, v72
	v_fma_f32 v71, v204, v212, -v71
	v_fma_f32 v73, v204, v213, v73
	v_cvt_pk_f16_f32 v219, v70, v71
	v_cvt_pk_f16_f32 v221, v72, v73
	v_xor_b32_e32 v255, 8, v254
	ds_read2_b64 v[206:209], v255 offset0:0 offset1:16
	ds_read2_b64 v[210:213], v255 offset0:32 offset1:48
	v_mfma_f32_32x32x16_f16 v[2:17], v[190:193], v[214:217], 0
	v_mfma_f32_32x32x16_f16 v[18:33], v[194:197], v[218:221], 0
	s_waitcnt lgkmcnt(0)
	v_mul_f32_e32 v66, v199, v207
	v_mul_f32_e32 v68, v199, v206
	v_mul_f32_e32 v67, v199, v209
	v_mul_f32_e32 v69, v199, v208
	v_fma_f32 v66, v198, v206, -v66
	v_fma_f32 v68, v198, v207, v68
	v_fma_f32 v67, v198, v208, -v67
	v_fma_f32 v69, v198, v209, v69
	v_cvt_pk_f16_f32 v214, v66, v67
	v_cvt_pk_f16_f32 v216, v68, v69
	v_mul_f32_e32 v70, v201, v211
	v_mul_f32_e32 v72, v201, v210
	v_mul_f32_e32 v71, v201, v213
	v_mul_f32_e32 v73, v201, v212
	v_fma_f32 v70, v200, v210, -v70
	v_fma_f32 v72, v200, v211, v72
	v_fma_f32 v71, v200, v212, -v71
	v_fma_f32 v73, v200, v213, v73
	v_cvt_pk_f16_f32 v215, v70, v71
	v_cvt_pk_f16_f32 v217, v72, v73
	v_cvt_pk_f16_f32 v2, v2, v3
	v_cvt_pk_f16_f32 v3, v4, v5
	v_cvt_pk_f16_f32 v4, v6, v7
	v_cvt_pk_f16_f32 v5, v8, v9
	v_cvt_pk_f16_f32 v6, v10, v11
	v_cvt_pk_f16_f32 v7, v12, v13
	v_cvt_pk_f16_f32 v8, v14, v15
	v_cvt_pk_f16_f32 v9, v16, v17
	v_cvt_pk_f16_f32 v18, v18, v19
	v_cvt_pk_f16_f32 v19, v20, v21
	v_cvt_pk_f16_f32 v20, v22, v23
	v_cvt_pk_f16_f32 v21, v24, v25
	v_cvt_pk_f16_f32 v22, v26, v27
	v_cvt_pk_f16_f32 v23, v28, v29
	v_cvt_pk_f16_f32 v24, v30, v31
	v_cvt_pk_f16_f32 v25, v32, v33
	s_setprio 1
	s_waitcnt vmcnt(6)
	v_mul_f32_e32 v66, v203, v207
	v_mul_f32_e32 v68, v203, v206
	v_mfma_f32_32x32x16_f16 v[34:49], v[2:5], v[150:153], 0
	v_mul_f32_e32 v67, v203, v209
	v_mul_f32_e32 v69, v203, v208
	v_mfma_f32_32x32x16_f16 v[34:49], v[18:21], v[146:149], v[34:49]
	v_fma_f32 v66, v202, v206, -v66
	v_fma_f32 v68, v202, v207, v68
	v_mfma_f32_32x32x16_f16 v[34:49], v[6:9], v[142:145], v[34:49]
	v_fma_f32 v67, v202, v208, -v67
	v_fma_f32 v69, v202, v209, v69
	v_mfma_f32_32x32x16_f16 v[34:49], v[22:25], v[138:141], v[34:49]
	v_cvt_pk_f16_f32 v218, v66, v67
	v_cvt_pk_f16_f32 v220, v68, v69
	s_waitcnt vmcnt(2)
	v_mul_f32_e32 v70, v205, v211
	v_mul_f32_e32 v72, v205, v210
	v_mfma_f32_32x32x16_f16 v[50:65], v[2:5], v[134:137], 0
	v_mul_f32_e32 v71, v205, v213
	v_mul_f32_e32 v73, v205, v212
	v_mfma_f32_32x32x16_f16 v[50:65], v[18:21], v[126:129], v[50:65]
	v_fma_f32 v70, v204, v210, -v70
	v_fma_f32 v72, v204, v211, v72
	v_mfma_f32_32x32x16_f16 v[50:65], v[6:9], v[122:125], v[50:65]
	v_fma_f32 v71, v204, v212, -v71
	v_fma_f32 v73, v204, v213, v73
	v_mfma_f32_32x32x16_f16 v[50:65], v[22:25], v[130:133], v[50:65]
	v_cvt_pk_f16_f32 v219, v70, v71
	v_cvt_pk_f16_f32 v221, v72, v73
	v_xor_b32_e32 v255, 16, v254
	ds_read2_b64 v[206:209], v255 offset0:0 offset1:16
	ds_read2_b64 v[210:213], v255 offset0:32 offset1:48
	v_mfma_f32_32x32x16_f16 v[2:17], v[190:193], v[214:217], 0
	v_mfma_f32_32x32x16_f16 v[18:33], v[194:197], v[218:221], 0
	v_cvt_pk_f16_f32 v34, v34, v35
	v_cvt_pk_f16_f32 v35, v36, v37
	v_cvt_pk_f16_f32 v36, v38, v39
	v_cvt_pk_f16_f32 v37, v40, v41
	v_cvt_pk_f16_f32 v38, v42, v43
	v_cvt_pk_f16_f32 v39, v44, v45
	v_cvt_pk_f16_f32 v40, v46, v47
	v_cvt_pk_f16_f32 v41, v48, v49
	v_cvt_pk_f16_f32 v50, v50, v51
	v_cvt_pk_f16_f32 v51, v52, v53
	v_cvt_pk_f16_f32 v52, v54, v55
	v_cvt_pk_f16_f32 v53, v56, v57
	v_cvt_pk_f16_f32 v54, v58, v59
	v_cvt_pk_f16_f32 v55, v60, v61
	v_cvt_pk_f16_f32 v56, v62, v63
	v_cvt_pk_f16_f32 v57, v64, v65
	s_waitcnt vmcnt(2)
	v_cvt_pk_f16_f32 v2, v2, v3
	v_cvt_pk_f16_f32 v3, v4, v5
	v_cvt_pk_f16_f32 v4, v6, v7
	v_cvt_pk_f16_f32 v5, v8, v9
	v_mfma_f32_32x32x16_f16 v[90:105], v[34:37], v[222:225], 0
	v_cvt_pk_f16_f32 v6, v10, v11
	v_cvt_pk_f16_f32 v7, v12, v13
	v_cvt_pk_f16_f32 v8, v14, v15
	v_cvt_pk_f16_f32 v9, v16, v17
	v_mfma_f32_32x32x16_f16 v[106:121], v[34:37], v[238:241], 0
	v_cvt_pk_f16_f32 v18, v18, v19
	v_cvt_pk_f16_f32 v19, v20, v21
	v_cvt_pk_f16_f32 v20, v22, v23
	v_cvt_pk_f16_f32 v21, v24, v25
	v_mfma_f32_32x32x16_f16 v[90:105], v[38:41], v[226:229], v[90:105]
	v_cvt_pk_f16_f32 v22, v26, v27
	v_cvt_pk_f16_f32 v23, v28, v29
	v_cvt_pk_f16_f32 v24, v30, v31
	v_cvt_pk_f16_f32 v25, v32, v33
	v_mfma_f32_32x32x16_f16 v[106:121], v[38:41], v[242:245], v[106:121]
	s_waitcnt lgkmcnt(0)
	v_mul_f32_e32 v66, v199, v207
	v_mul_f32_e32 v68, v199, v206
	v_mul_f32_e32 v67, v199, v209
	v_mfma_f32_32x32x16_f16 v[90:105], v[50:53], v[230:233], v[90:105]
	v_mul_f32_e32 v69, v199, v208
	v_fma_f32 v66, v198, v206, -v66
	v_fma_f32 v68, v198, v207, v68
	v_fma_f32 v67, v198, v208, -v67
	v_mfma_f32_32x32x16_f16 v[106:121], v[50:53], v[246:249], v[106:121]
	v_fma_f32 v69, v198, v209, v69
	v_cvt_pk_f16_f32 v214, v66, v67
	v_cvt_pk_f16_f32 v216, v68, v69
	v_mul_f32_e32 v70, v201, v211
	v_mfma_f32_32x32x16_f16 v[90:105], v[54:57], v[234:237], v[90:105]
	v_mul_f32_e32 v72, v201, v210
	v_mul_f32_e32 v71, v201, v213
	v_mul_f32_e32 v73, v201, v212
	v_fma_f32 v70, v200, v210, -v70
	v_mfma_f32_32x32x16_f16 v[106:121], v[54:57], v[250:253], v[106:121]
	v_fma_f32 v72, v200, v211, v72
	v_fma_f32 v71, v200, v212, -v71
	v_fma_f32 v73, v200, v213, v73
	v_cvt_pk_f16_f32 v215, v70, v71
	v_cvt_pk_f16_f32 v217, v72, v73
	v_mfma_f32_32x32x16_f16 v[34:49], v[2:5], v[150:153], 0
	v_mul_f32_e32 v66, v203, v207
	v_mul_f32_e32 v68, v203, v206
	v_mul_f32_e32 v67, v203, v209
	v_mul_f32_e32 v69, v203, v208
	v_fma_f32 v66, v202, v206, -v66
	v_mfma_f32_32x32x16_f16 v[34:49], v[18:21], v[146:149], v[34:49]
	v_fma_f32 v68, v202, v207, v68
	v_fma_f32 v67, v202, v208, -v67
	v_fma_f32 v69, v202, v209, v69
	v_cvt_pk_f16_f32 v218, v66, v67
	v_cvt_pk_f16_f32 v220, v68, v69
	v_mfma_f32_32x32x16_f16 v[34:49], v[6:9], v[142:145], v[34:49]
	v_mul_f32_e32 v70, v205, v211
	v_mul_f32_e32 v72, v205, v210
	v_mul_f32_e32 v71, v205, v213
	v_mul_f32_e32 v73, v205, v212
	v_fma_f32 v70, v204, v210, -v70
	v_mfma_f32_32x32x16_f16 v[34:49], v[22:25], v[138:141], v[34:49]
	v_fma_f32 v72, v204, v211, v72
	v_fma_f32 v71, v204, v212, -v71
	v_fma_f32 v73, v204, v213, v73
	v_cvt_pk_f16_f32 v219, v70, v71
	v_cvt_pk_f16_f32 v221, v72, v73
	v_mfma_f32_32x32x16_f16 v[50:65], v[2:5], v[134:137], 0
	v_cvt_pk_f16_f32 v90, v90, v91
	v_cvt_pk_f16_f32 v91, v92, v93
	v_cvt_pk_f16_f32 v92, v94, v95
	v_cvt_pk_f16_f32 v93, v96, v97
	v_cvt_pk_f16_f32 v94, v98, v99
	v_mfma_f32_32x32x16_f16 v[50:65], v[18:21], v[126:129], v[50:65]
	v_cvt_pk_f16_f32 v95, v100, v101
	v_cvt_pk_f16_f32 v96, v102, v103
	v_cvt_pk_f16_f32 v97, v104, v105
	v_cvt_pk_f16_f32 v106, v106, v107
	v_cvt_pk_f16_f32 v107, v108, v109
	v_mfma_f32_32x32x16_f16 v[50:65], v[6:9], v[122:125], v[50:65]
	v_cvt_pk_f16_f32 v108, v110, v111
	v_cvt_pk_f16_f32 v109, v112, v113
	v_cvt_pk_f16_f32 v110, v114, v115
	v_cvt_pk_f16_f32 v111, v116, v117
	v_cvt_pk_f16_f32 v112, v118, v119
	v_mfma_f32_32x32x16_f16 v[50:65], v[22:25], v[130:133], v[50:65]
	v_cvt_pk_f16_f32 v113, v120, v121
	ds_write_b128 v173, v[90:93]
	ds_write_b128 v172, v[94:97]
	ds_write_b128 v173, v[106:109] offset:32768
	ds_write_b128 v172, v[110:113] offset:32768
	v_xor_b32_e32 v255, 24, v254
	ds_read2_b64 v[206:209], v255 offset0:0 offset1:16
	ds_read2_b64 v[210:213], v255 offset0:32 offset1:48
	v_mfma_f32_32x32x16_f16 v[2:17], v[190:193], v[214:217], 0
	v_mfma_f32_32x32x16_f16 v[18:33], v[194:197], v[218:221], 0
	v_cvt_pk_f16_f32 v34, v34, v35
	v_cvt_pk_f16_f32 v35, v36, v37
	v_cvt_pk_f16_f32 v36, v38, v39
	v_cvt_pk_f16_f32 v37, v40, v41
	v_cvt_pk_f16_f32 v38, v42, v43
	v_cvt_pk_f16_f32 v39, v44, v45
	v_cvt_pk_f16_f32 v40, v46, v47
	v_cvt_pk_f16_f32 v41, v48, v49
	v_cvt_pk_f16_f32 v50, v50, v51
	v_cvt_pk_f16_f32 v51, v52, v53
	v_cvt_pk_f16_f32 v52, v54, v55
	v_cvt_pk_f16_f32 v53, v56, v57
	v_cvt_pk_f16_f32 v54, v58, v59
	v_cvt_pk_f16_f32 v55, v60, v61
	v_cvt_pk_f16_f32 v56, v62, v63
	v_cvt_pk_f16_f32 v57, v64, v65
	v_mfma_f32_32x32x16_f16 v[90:105], v[34:37], v[222:225], 0
	v_cvt_pk_f16_f32 v2, v2, v3
	v_cvt_pk_f16_f32 v3, v4, v5
	v_cvt_pk_f16_f32 v4, v6, v7
	v_cvt_pk_f16_f32 v5, v8, v9
	v_mfma_f32_32x32x16_f16 v[106:121], v[34:37], v[238:241], 0
	v_cvt_pk_f16_f32 v6, v10, v11
	v_cvt_pk_f16_f32 v7, v12, v13
	v_cvt_pk_f16_f32 v8, v14, v15
	v_cvt_pk_f16_f32 v9, v16, v17
	v_cvt_pk_f16_f32 v18, v18, v19
	v_mfma_f32_32x32x16_f16 v[90:105], v[38:41], v[226:229], v[90:105]
	v_cvt_pk_f16_f32 v19, v20, v21
	v_cvt_pk_f16_f32 v20, v22, v23
	v_cvt_pk_f16_f32 v21, v24, v25
	v_cvt_pk_f16_f32 v22, v26, v27
	v_mfma_f32_32x32x16_f16 v[106:121], v[38:41], v[242:245], v[106:121]
	v_cvt_pk_f16_f32 v23, v28, v29
	v_cvt_pk_f16_f32 v24, v30, v31
	v_cvt_pk_f16_f32 v25, v32, v33
	s_waitcnt lgkmcnt(0)
	v_mul_f32_e32 v66, v199, v207
	v_mfma_f32_32x32x16_f16 v[90:105], v[50:53], v[230:233], v[90:105]
	v_mul_f32_e32 v68, v199, v206
	v_mul_f32_e32 v67, v199, v209
	v_mul_f32_e32 v69, v199, v208
	v_fma_f32 v66, v198, v206, -v66
	v_fma_f32 v68, v198, v207, v68
	v_mfma_f32_32x32x16_f16 v[106:121], v[50:53], v[246:249], v[106:121]
	v_fma_f32 v67, v198, v208, -v67
	v_fma_f32 v69, v198, v209, v69
	v_cvt_pk_f16_f32 v214, v66, v67
	v_cvt_pk_f16_f32 v216, v68, v69
	v_mfma_f32_32x32x16_f16 v[90:105], v[54:57], v[234:237], v[90:105]
	v_mul_f32_e32 v70, v201, v211
	v_mul_f32_e32 v72, v201, v210
	v_mul_f32_e32 v71, v201, v213
	v_mul_f32_e32 v73, v201, v212
	v_fma_f32 v70, v200, v210, -v70
	v_mfma_f32_32x32x16_f16 v[106:121], v[54:57], v[250:253], v[106:121]
	v_fma_f32 v72, v200, v211, v72
	v_fma_f32 v71, v200, v212, -v71
	v_fma_f32 v73, v200, v213, v73
	v_cvt_pk_f16_f32 v215, v70, v71
	v_cvt_pk_f16_f32 v217, v72, v73
	v_mfma_f32_32x32x16_f16 v[34:49], v[2:5], v[150:153], 0
	v_mul_f32_e32 v66, v203, v207
	v_mul_f32_e32 v68, v203, v206
	v_mul_f32_e32 v67, v203, v209
	v_mul_f32_e32 v69, v203, v208
	v_fma_f32 v66, v202, v206, -v66
	v_mfma_f32_32x32x16_f16 v[34:49], v[18:21], v[146:149], v[34:49]
	v_fma_f32 v68, v202, v207, v68
	v_fma_f32 v67, v202, v208, -v67
	v_fma_f32 v69, v202, v209, v69
	v_cvt_pk_f16_f32 v218, v66, v67
	v_cvt_pk_f16_f32 v220, v68, v69
	v_mfma_f32_32x32x16_f16 v[34:49], v[6:9], v[142:145], v[34:49]
	v_mul_f32_e32 v70, v205, v211
	v_mul_f32_e32 v72, v205, v210
	v_mul_f32_e32 v71, v205, v213
	v_mul_f32_e32 v73, v205, v212
	v_fma_f32 v70, v204, v210, -v70
	v_mfma_f32_32x32x16_f16 v[34:49], v[22:25], v[138:141], v[34:49]
	v_fma_f32 v72, v204, v211, v72
	v_fma_f32 v71, v204, v212, -v71
	v_fma_f32 v73, v204, v213, v73
	v_cvt_pk_f16_f32 v219, v70, v71
	v_cvt_pk_f16_f32 v221, v72, v73
	v_cvt_pk_f16_f32 v90, v90, v91
	v_mfma_f32_32x32x16_f16 v[50:65], v[2:5], v[134:137], 0
	v_cvt_pk_f16_f32 v91, v92, v93
	v_cvt_pk_f16_f32 v92, v94, v95
	v_cvt_pk_f16_f32 v93, v96, v97
	v_cvt_pk_f16_f32 v94, v98, v99
	v_cvt_pk_f16_f32 v95, v100, v101
	v_mfma_f32_32x32x16_f16 v[50:65], v[18:21], v[126:129], v[50:65]
	v_cvt_pk_f16_f32 v96, v102, v103
	v_cvt_pk_f16_f32 v97, v104, v105
	v_cvt_pk_f16_f32 v106, v106, v107
	v_cvt_pk_f16_f32 v107, v108, v109
	v_cvt_pk_f16_f32 v108, v110, v111
	v_mfma_f32_32x32x16_f16 v[50:65], v[6:9], v[122:125], v[50:65]
	v_cvt_pk_f16_f32 v109, v112, v113
	v_cvt_pk_f16_f32 v110, v114, v115
	v_cvt_pk_f16_f32 v111, v116, v117
	v_cvt_pk_f16_f32 v112, v118, v119
	v_cvt_pk_f16_f32 v113, v120, v121
	v_mfma_f32_32x32x16_f16 v[50:65], v[22:25], v[130:133], v[50:65]
	v_xor_b32_e32 v74, 0x8a0, v173
	v_xor_b32_e32 v75, 0x8a0, v172
	ds_write_b128 v74, v[90:93]
	ds_write_b128 v75, v[94:97]
	ds_write_b128 v74, v[106:109] offset:32768
	ds_write_b128 v75, v[110:113] offset:32768
	s_nop 0
	v_mfma_f32_32x32x16_f16 v[2:17], v[190:193], v[214:217], 0
	v_mfma_f32_32x32x16_f16 v[18:33], v[194:197], v[218:221], 0
	v_cvt_pk_f16_f32 v34, v34, v35
	v_cvt_pk_f16_f32 v35, v36, v37
	v_cvt_pk_f16_f32 v36, v38, v39
	v_cvt_pk_f16_f32 v37, v40, v41
	v_cvt_pk_f16_f32 v38, v42, v43
	v_cvt_pk_f16_f32 v39, v44, v45
	v_cvt_pk_f16_f32 v40, v46, v47
	v_cvt_pk_f16_f32 v41, v48, v49
	v_cvt_pk_f16_f32 v50, v50, v51
	v_cvt_pk_f16_f32 v51, v52, v53
	v_cvt_pk_f16_f32 v52, v54, v55
	v_cvt_pk_f16_f32 v53, v56, v57
	v_cvt_pk_f16_f32 v54, v58, v59
	v_cvt_pk_f16_f32 v55, v60, v61
	v_cvt_pk_f16_f32 v56, v62, v63
	v_cvt_pk_f16_f32 v57, v64, v65
	v_mfma_f32_32x32x16_f16 v[90:105], v[34:37], v[222:225], 0
	v_cvt_pk_f16_f32 v2, v2, v3
	v_cvt_pk_f16_f32 v3, v4, v5
	v_mfma_f32_32x32x16_f16 v[106:121], v[34:37], v[238:241], 0
	v_cvt_pk_f16_f32 v4, v6, v7
	v_cvt_pk_f16_f32 v5, v8, v9
	v_mfma_f32_32x32x16_f16 v[90:105], v[38:41], v[226:229], v[90:105]
	v_cvt_pk_f16_f32 v6, v10, v11
	v_cvt_pk_f16_f32 v7, v12, v13
	v_mfma_f32_32x32x16_f16 v[106:121], v[38:41], v[242:245], v[106:121]
	v_cvt_pk_f16_f32 v8, v14, v15
	v_cvt_pk_f16_f32 v9, v16, v17
	v_mfma_f32_32x32x16_f16 v[90:105], v[50:53], v[230:233], v[90:105]
	v_cvt_pk_f16_f32 v18, v18, v19
	v_cvt_pk_f16_f32 v19, v20, v21
	v_mfma_f32_32x32x16_f16 v[106:121], v[50:53], v[246:249], v[106:121]
	v_cvt_pk_f16_f32 v20, v22, v23
	v_cvt_pk_f16_f32 v21, v24, v25
	v_mfma_f32_32x32x16_f16 v[90:105], v[54:57], v[234:237], v[90:105]
	v_cvt_pk_f16_f32 v22, v26, v27
	v_cvt_pk_f16_f32 v23, v28, v29
	v_mfma_f32_32x32x16_f16 v[106:121], v[54:57], v[250:253], v[106:121]
	v_cvt_pk_f16_f32 v24, v30, v31
	v_cvt_pk_f16_f32 v25, v32, v33
	v_mfma_f32_32x32x16_f16 v[34:49], v[2:5], v[150:153], 0
	v_mfma_f32_32x32x16_f16 v[34:49], v[18:21], v[146:149], v[34:49]
	v_mfma_f32_32x32x16_f16 v[34:49], v[6:9], v[142:145], v[34:49]
	v_mfma_f32_32x32x16_f16 v[34:49], v[22:25], v[138:141], v[34:49]
	v_mfma_f32_32x32x16_f16 v[50:65], v[2:5], v[134:137], 0
	s_nop 5
	v_cvt_pk_f16_f32 v90, v90, v91
	v_cvt_pk_f16_f32 v91, v92, v93
	v_cvt_pk_f16_f32 v92, v94, v95
	v_cvt_pk_f16_f32 v93, v96, v97
	v_mfma_f32_32x32x16_f16 v[50:65], v[18:21], v[126:129], v[50:65]
	v_cvt_pk_f16_f32 v94, v98, v99
	v_cvt_pk_f16_f32 v95, v100, v101
	v_cvt_pk_f16_f32 v96, v102, v103
	v_cvt_pk_f16_f32 v97, v104, v105
	v_cvt_pk_f16_f32 v106, v106, v107
	v_cvt_pk_f16_f32 v107, v108, v109
	v_mfma_f32_32x32x16_f16 v[50:65], v[6:9], v[122:125], v[50:65]
	v_cvt_pk_f16_f32 v108, v110, v111
	v_cvt_pk_f16_f32 v109, v112, v113
	v_cvt_pk_f16_f32 v110, v114, v115
	v_cvt_pk_f16_f32 v111, v116, v117
	v_cvt_pk_f16_f32 v112, v118, v119
	v_cvt_pk_f16_f32 v113, v120, v121
	v_mfma_f32_32x32x16_f16 v[50:65], v[22:25], v[130:133], v[50:65]
	v_xor_b32_e32 v74, 0x1040, v173
	v_xor_b32_e32 v75, 0x1040, v172
	ds_write_b128 v74, v[90:93]
	ds_write_b128 v75, v[94:97]
	ds_write_b128 v74, v[106:109] offset:32768
	ds_write_b128 v75, v[110:113] offset:32768
	s_nop 11
	v_cvt_pk_f16_f32 v34, v34, v35
	v_cvt_pk_f16_f32 v35, v36, v37
	v_cvt_pk_f16_f32 v36, v38, v39
	v_cvt_pk_f16_f32 v37, v40, v41
	v_cvt_pk_f16_f32 v38, v42, v43
	v_cvt_pk_f16_f32 v39, v44, v45
	v_cvt_pk_f16_f32 v40, v46, v47
	v_cvt_pk_f16_f32 v41, v48, v49
	v_cvt_pk_f16_f32 v50, v50, v51
	v_cvt_pk_f16_f32 v51, v52, v53
	v_cvt_pk_f16_f32 v52, v54, v55
	v_cvt_pk_f16_f32 v53, v56, v57
	v_cvt_pk_f16_f32 v54, v58, v59
	v_cvt_pk_f16_f32 v55, v60, v61
	v_cvt_pk_f16_f32 v56, v62, v63
	v_cvt_pk_f16_f32 v57, v64, v65
	v_mfma_f32_32x32x16_f16 v[90:105], v[34:37], v[222:225], 0
	v_mfma_f32_32x32x16_f16 v[106:121], v[34:37], v[238:241], 0
	v_mfma_f32_32x32x16_f16 v[90:105], v[38:41], v[226:229], v[90:105]
	v_mfma_f32_32x32x16_f16 v[106:121], v[38:41], v[242:245], v[106:121]
	v_mfma_f32_32x32x16_f16 v[90:105], v[50:53], v[230:233], v[90:105]
	v_mfma_f32_32x32x16_f16 v[106:121], v[50:53], v[246:249], v[106:121]
	v_mfma_f32_32x32x16_f16 v[90:105], v[54:57], v[234:237], v[90:105]
	v_mfma_f32_32x32x16_f16 v[106:121], v[54:57], v[250:253], v[106:121]
	v_and_b32_e32 v134, 1, v156
	v_bitop3_b32 v132, v171, s40, v170 bitop3:0x36
	v_bitop3_b32 v131, s41, v154, v160 bitop3:0x36
	v_bitop3_b32 v135, v171, s42, v170 bitop3:0x36
	v_xor_b32_e32 v133, s43, v154
	v_and_b32_e32 v130, 4, v156
	s_lshl_b32 s2, s27, 3
	s_lshl_b32 s3, s5, 2
	s_or_b32 s2, s3, s2
	s_ashr_i32 s3, s2, 31
	s_lshl_b64 s[2:3], s[2:3], 13
	s_add_u32 s2, s20, s2
	s_addc_u32 s3, s21, s3
	v_lshlrev_b32_e32 v154, 1, v169
	v_lshl_add_u64 v[2:3], s[2:3], 0, v[154:155]
	v_add_co_u32_e32 v2, vcc, s23, v2
	s_nop 1
	v_addc_co_u32_e32 v3, vcc, 0, v3, vcc
	v_cvt_pk_f16_f32 v90, v90, v91
	v_cvt_pk_f16_f32 v91, v92, v93
	v_cvt_pk_f16_f32 v92, v94, v95
	v_cvt_pk_f16_f32 v93, v96, v97
	v_cvt_pk_f16_f32 v94, v98, v99
	v_cvt_pk_f16_f32 v95, v100, v101
	v_cvt_pk_f16_f32 v96, v102, v103
	v_cvt_pk_f16_f32 v97, v104, v105
	v_cvt_pk_f16_f32 v106, v106, v107
	v_cvt_pk_f16_f32 v107, v108, v109
	v_cvt_pk_f16_f32 v108, v110, v111
	v_cvt_pk_f16_f32 v109, v112, v113
	v_cvt_pk_f16_f32 v110, v114, v115
	v_cvt_pk_f16_f32 v111, v116, v117
	v_cvt_pk_f16_f32 v112, v118, v119
	v_cvt_pk_f16_f32 v113, v120, v121
	v_xor_b32_e32 v74, 0x18e0, v173
	v_xor_b32_e32 v75, 0x18e0, v172
	ds_write_b128 v74, v[90:93]
	ds_write_b128 v75, v[94:97]
	ds_write_b128 v74, v[106:109] offset:32768
	ds_write_b128 v75, v[110:113] offset:32768
	s_setprio 0
	s_waitcnt lgkmcnt(0)
	s_barrier
	global_load_dwordx4 v[62:65], v154, s[2:3]
	global_load_dwordx4 v[46:49], v154, s[2:3] offset:1024
	global_load_dwordx4 v[42:45], v154, s[2:3] offset:2048
	global_load_dwordx4 v[38:41], v154, s[2:3] offset:3072
	global_load_dwordx4 v[54:57], v[2:3], off offset:1024
	global_load_dwordx4 v[50:53], v[2:3], off offset:2048
	v_lshl_add_u64 v[4:5], s[12:13], 0, v[154:155]
	global_load_dwordx4 v[126:129], v154, s[12:13]
	global_load_dwordx4 v[122:125], v154, s[12:13] offset:1024
	global_load_dwordx4 v[118:121], v154, s[12:13] offset:2048
	global_load_dwordx4 v[114:117], v154, s[12:13] offset:3072
	global_load_dwordx4 v[34:37], v168, s[2:3]
	global_load_dwordx4 v[110:113], v168, s[12:13]
	v_add_co_u32_e32 v4, vcc, s23, v4
	s_nop 1
	v_addc_co_u32_e32 v5, vcc, 0, v5, vcc
	global_load_dwordx4 v[58:61], v[2:3], off offset:3072
	global_load_dwordx4 v[106:109], v[4:5], off offset:1024
	global_load_dwordx4 v[94:97], v[4:5], off offset:2048
	global_load_dwordx4 v[90:93], v[4:5], off offset:3072
	v_bfrev_b32_e32 v3, v156
	v_lshlrev_b32_e32 v7, 5, v167
	v_lshlrev_b32_e32 v6, 9, v167
	v_and_b32_e32 v7, 0x200, v7
	v_lshlrev_b32_e32 v8, 8, v167
	v_lshrrev_b32_e32 v3, 27, v3
	v_lshrrev_b32_e32 v2, 2, v167
	v_lshrrev_b32_e32 v4, 4, v156
	v_xor_b32_e32 v5, v169, v156
	v_and_b32_e32 v6, 0x5800, v6
	v_and_b32_e32 v3, 8, v3
	v_and_or_b32 v7, v8, s24, v7
	v_lshrrev_b32_e32 v5, 1, v5
	v_xor_b32_e32 v4, v2, v4
	v_or3_b32 v3, v7, v6, v3
	v_bitop3_b32 v7, v2, v182, 1 bitop3:0x6c
	v_lshlrev_b32_e32 v2, 1, v167
	v_and_b32_e32 v5, 4, v5
	v_lshlrev_b32_e32 v4, 3, v4
	v_lshrrev_b32_e32 v6, 1, v167
	v_and_b32_e32 v2, 2, v2
	v_and_or_b32 v9, v169, 8, v2
	v_and_b32_e32 v2, 8, v4
	v_and_or_b32 v4, v6, 2, v5
	v_or3_b32 v2, v4, v2, v134
	v_lshlrev_b32_e32 v2, 4, v2
	v_bitop3_b32 v146, v3, s28, v2 bitop3:0x36
	v_xor_b32_e32 v8, v6, v182
	v_xor_b32_e32 v147, 0x2010, v146
	ds_read_b64_tr_b16 v[2:3], v146
	ds_read_b64_tr_b16 v[4:5], v147
	v_lshlrev_b32_e32 v8, 2, v8
	v_and_b32_e32 v8, 4, v8
	v_or3_b32 v6, v9, v7, v8
	v_lshlrev_b32_e32 v7, 11, v167
	v_and_b32_e32 v8, 0x7800, v7
	v_lshlrev_b32_e32 v6, 4, v6
	v_or3_b32 v22, v6, v8, v170
	v_and_b32_e32 v23, 0x8000, v7
	s_waitcnt vmcnt(17) lgkmcnt(0)
	v_mfma_f32_32x32x16_f16 v[2:17], v[2:5], v[86:89], 0
	ds_read_b64_tr_b16 v[20:21], v147 offset:32768
	ds_read_b64_tr_b16 v[18:19], v146 offset:32768
	v_xor_b32_e32 v150, 16, v146
	v_xad_u32 v70, v22, s28, v23
	v_xor_b32_e32 v151, 0x2000, v146
	ds_read_b64_tr_b16 v[22:23], v150
	ds_read_b64_tr_b16 v[24:25], v151
	ds_read_b64_tr_b16 v[28:29], v151 offset:32768
	ds_read_b64_tr_b16 v[26:27], v150 offset:32768
	v_xor_b32_e32 v30, 0x280, v70
	v_xor_b32_e32 v148, 32, v146
	s_waitcnt vmcnt(16) lgkmcnt(4)
	v_mfma_f32_32x32x16_f16 v[2:17], v[18:21], v[82:85], v[2:17]
	v_xor_b32_e32 v149, 0x2030, v146
	v_xor_b32_e32 v144, 48, v146
	v_xor_b32_e32 v145, 0x2020, v146
	v_xor_b32_e32 v142, 64, v146
	v_xor_b32_e32 v143, 0x2050, v146
	v_xor_b32_e32 v140, 0x50, v146
	v_xor_b32_e32 v141, 0x2040, v146
	s_nop 4
	v_cvt_pk_f16_f32 v9, v8, v9
	v_cvt_pk_f16_f32 v8, v6, v7
	v_cvt_pk_f16_f32 v7, v4, v5
	v_cvt_pk_f16_f32 v6, v2, v3
	ds_write_b128 v70, v[6:9]
	v_cvt_pk_f16_f32 v21, v16, v17
	v_cvt_pk_f16_f32 v20, v14, v15
	v_cvt_pk_f16_f32 v19, v12, v13
	v_cvt_pk_f16_f32 v18, v10, v11
	s_waitcnt lgkmcnt(3)
	v_mfma_f32_32x32x16_f16 v[2:17], v[22:25], v[86:89], 0
	ds_write_b128 v30, v[18:21]
	ds_read_b64_tr_b16 v[18:19], v148
	ds_read_b64_tr_b16 v[20:21], v149
	ds_read_b64_tr_b16 v[24:25], v149 offset:32768
	ds_read_b64_tr_b16 v[22:23], v148 offset:32768
	v_xor_b32_e32 v30, 0x290, v70
	v_xor_b32_e32 v138, 0x60, v146
	v_xor_b32_e32 v139, 0x2070, v146
	v_xor_b32_e32 v136, 0x70, v146
	v_xor_b32_e32 v137, 0x2060, v146
	s_waitcnt lgkmcnt(6)
	v_mfma_f32_32x32x16_f16 v[2:17], v[26:29], v[82:85], v[2:17]
	v_xor_b32_e32 v26, 16, v70
	v_xor_b32_e32 v71, 0x60, v70
	s_lshl_b64 s[0:1], s[0:1], 13
	s_add_u32 s0, s8, s0
	s_addc_u32 s1, s9, s1
	s_nop 6
	v_cvt_pk_f16_f32 v9, v8, v9
	v_cvt_pk_f16_f32 v8, v6, v7
	v_cvt_pk_f16_f32 v7, v4, v5
	v_cvt_pk_f16_f32 v6, v2, v3
	ds_write_b128 v26, v[6:9]
	v_cvt_pk_f16_f32 v29, v16, v17
	v_cvt_pk_f16_f32 v28, v14, v15
	v_cvt_pk_f16_f32 v27, v12, v13
	v_cvt_pk_f16_f32 v26, v10, v11
	s_waitcnt lgkmcnt(3)
	v_mfma_f32_32x32x16_f16 v[2:17], v[18:21], v[86:89], 0
	ds_write_b128 v30, v[26:29]
	ds_read_b64_tr_b16 v[18:19], v144
	ds_read_b64_tr_b16 v[20:21], v145
	ds_read_b64_tr_b16 v[28:29], v145 offset:32768
	ds_read_b64_tr_b16 v[26:27], v144 offset:32768
	v_xor_b32_e32 v30, 0x2a0, v70
	s_waitcnt lgkmcnt(6)
	v_mfma_f32_32x32x16_f16 v[2:17], v[22:25], v[82:85], v[2:17]
	v_xor_b32_e32 v22, 32, v70
	s_nop 10
	v_cvt_pk_f16_f32 v9, v8, v9
	v_cvt_pk_f16_f32 v8, v6, v7
	v_cvt_pk_f16_f32 v7, v4, v5
	v_cvt_pk_f16_f32 v6, v2, v3
	ds_write_b128 v22, v[6:9]
	v_cvt_pk_f16_f32 v25, v16, v17
	v_cvt_pk_f16_f32 v24, v14, v15
	v_cvt_pk_f16_f32 v23, v12, v13
	v_cvt_pk_f16_f32 v22, v10, v11
	s_waitcnt lgkmcnt(3)
	v_mfma_f32_32x32x16_f16 v[2:17], v[18:21], v[86:89], 0
	ds_write_b128 v30, v[22:25]
	ds_read_b64_tr_b16 v[18:19], v142
	ds_read_b64_tr_b16 v[20:21], v143
	ds_read_b64_tr_b16 v[24:25], v143 offset:32768
	ds_read_b64_tr_b16 v[22:23], v142 offset:32768
	v_xor_b32_e32 v30, 0x2b0, v70
	s_waitcnt lgkmcnt(6)
	v_mfma_f32_32x32x16_f16 v[2:17], v[26:29], v[82:85], v[2:17]
	v_xor_b32_e32 v26, 48, v70
	s_nop 10
	v_cvt_pk_f16_f32 v9, v8, v9
	v_cvt_pk_f16_f32 v8, v6, v7
	v_cvt_pk_f16_f32 v7, v4, v5
	v_cvt_pk_f16_f32 v6, v2, v3
	ds_write_b128 v26, v[6:9]
	v_cvt_pk_f16_f32 v29, v16, v17
	v_cvt_pk_f16_f32 v28, v14, v15
	v_cvt_pk_f16_f32 v27, v12, v13
	v_cvt_pk_f16_f32 v26, v10, v11
	s_waitcnt lgkmcnt(3)
	v_mfma_f32_32x32x16_f16 v[2:17], v[18:21], v[86:89], 0
	ds_write_b128 v30, v[26:29]
	ds_read_b64_tr_b16 v[18:19], v140
	ds_read_b64_tr_b16 v[20:21], v141
	ds_read_b64_tr_b16 v[28:29], v141 offset:32768
	ds_read_b64_tr_b16 v[26:27], v140 offset:32768
	s_waitcnt lgkmcnt(6)
	v_mfma_f32_32x32x16_f16 v[2:17], v[22:25], v[82:85], v[2:17]
	v_xor_b32_e32 v22, 64, v70
	s_nop 10
	v_cvt_pk_f16_f32 v9, v8, v9
	v_cvt_pk_f16_f32 v8, v6, v7
	v_cvt_pk_f16_f32 v7, v4, v5
	v_cvt_pk_f16_f32 v6, v2, v3
	ds_write_b128 v22, v[6:9]
	v_cvt_pk_f16_f32 v5, v16, v17
	v_cvt_pk_f16_f32 v4, v14, v15
	v_cvt_pk_f16_f32 v3, v12, v13
	v_cvt_pk_f16_f32 v2, v10, v11
	s_waitcnt lgkmcnt(3)
	v_mfma_f32_32x32x16_f16 v[10:25], v[18:21], v[86:89], 0
	v_xor_b32_e32 v6, 0x2c0, v70
	ds_write_b128 v6, v[2:5]
	ds_read_b64_tr_b16 v[2:3], v138
	ds_read_b64_tr_b16 v[4:5], v139
	ds_read_b64_tr_b16 v[32:33], v139 offset:32768
	ds_read_b64_tr_b16 v[30:31], v138 offset:32768
	s_waitcnt lgkmcnt(6)
	v_mfma_f32_32x32x16_f16 v[10:25], v[26:29], v[82:85], v[10:25]
	v_xor_b32_e32 v26, 0x50, v70
	s_nop 10
	v_cvt_pk_f16_f32 v9, v16, v17
	v_cvt_pk_f16_f32 v8, v14, v15
	v_cvt_pk_f16_f32 v7, v12, v13
	v_cvt_pk_f16_f32 v6, v10, v11
	ds_write_b128 v26, v[6:9]
	s_waitcnt lgkmcnt(3)
	v_mfma_f32_32x32x16_f16 v[2:17], v[2:5], v[86:89], 0
	v_cvt_pk_f16_f32 v25, v24, v25
	v_cvt_pk_f16_f32 v24, v22, v23
	v_cvt_pk_f16_f32 v23, v20, v21
	v_cvt_pk_f16_f32 v22, v18, v19
	v_xor_b32_e32 v18, 0x2d0, v70
	ds_write_b128 v18, v[22:25]
	ds_read_b64_tr_b16 v[18:19], v136
	ds_read_b64_tr_b16 v[20:21], v137
	s_waitcnt lgkmcnt(4)
	v_mfma_f32_32x32x16_f16 v[2:17], v[30:33], v[82:85], v[2:17]
	ds_read_b64_tr_b16 v[68:69], v137 offset:32768
	ds_read_b64_tr_b16 v[66:67], v136 offset:32768
	s_waitcnt lgkmcnt(2)
	v_mfma_f32_32x32x16_f16 v[18:33], v[18:21], v[86:89], 0
	s_nop 7
	v_cvt_pk_f16_f32 v9, v8, v9
	v_cvt_pk_f16_f32 v8, v6, v7
	v_cvt_pk_f16_f32 v7, v4, v5
	v_cvt_pk_f16_f32 v6, v2, v3
	ds_write_b128 v71, v[6:9]
	v_cvt_pk_f16_f32 v5, v16, v17
	v_cvt_pk_f16_f32 v4, v14, v15
	s_waitcnt lgkmcnt(1)
	v_mfma_f32_32x32x16_f16 v[18:33], v[66:69], v[82:85], v[18:33]
	v_cvt_pk_f16_f32 v3, v12, v13
	v_cvt_pk_f16_f32 v2, v10, v11
	v_xor_b32_e32 v6, 0x2e0, v70
	ds_write_b128 v6, v[2:5]
	v_xor_b32_e32 v6, 0x70, v70
	s_nop 6
	v_cvt_pk_f16_f32 v5, v24, v25
	v_cvt_pk_f16_f32 v4, v22, v23
	v_cvt_pk_f16_f32 v3, v20, v21
	v_cvt_pk_f16_f32 v2, v18, v19
	ds_write_b128 v6, v[2:5]
	v_cvt_pk_f16_f32 v5, v32, v33
	v_cvt_pk_f16_f32 v4, v30, v31
	v_cvt_pk_f16_f32 v3, v28, v29
	v_cvt_pk_f16_f32 v2, v26, v27
	v_xor_b32_e32 v6, 0x2f0, v70
	ds_write_b128 v6, v[2:5]
	v_lshl_add_u64 v[2:3], s[0:1], 0, v[154:155]
	v_lshl_add_u64 v[4:5], v[2:3], 0, s[18:19]
	v_add_co_u32_e32 v2, vcc, s25, v2
	s_waitcnt lgkmcnt(0)
	s_nop 0
	v_addc_co_u32_e32 v3, vcc, 0, v3, vcc
	s_barrier
	s_nop 0
	s_nop 0
	global_load_dwordx4 v[102:105], v[2:3], off
	global_load_dwordx4 v[98:101], v[4:5], off offset:1024
	s_setprio 1
	s_add_u32 s0, s2, 0x2000
	s_addc_u32 s1, s3, 0
	v_lshl_add_u64 v[2:3], s[0:1], 0, v[154:155]
	v_add_co_u32_e32 v2, vcc, s23, v2
	global_load_dwordx4 v[66:69], v154, s[0:1]
	global_load_dwordx4 v[70:73], v154, s[0:1] offset:1024
	global_load_dwordx4 v[74:77], v154, s[0:1] offset:2048
	global_load_dwordx4 v[78:81], v154, s[0:1] offset:3072
	v_addc_co_u32_e32 v3, vcc, 0, v3, vcc
	global_load_dwordx4 v[82:85], v168, s[0:1]
	global_load_dwordx4 v[86:89], v[2:3], off offset:1024
	global_load_dwordx4 v[182:185], v[2:3], off offset:2048
	global_load_dwordx4 v[186:189], v[2:3], off offset:3072
	ds_read_b128 v[18:21], v179
	ds_read_b128 v[22:25], v179 offset:32768
	ds_read_b128 v[26:29], v178
	ds_read_b128 v[30:33], v178 offset:32768
	s_add_u32 s0, s2, 0x6000
	s_addc_u32 s1, s3, 0
	s_waitcnt vmcnt(25) lgkmcnt(3)
	v_mfma_f32_32x32x16_f16 v[2:17], v[18:21], v[62:65], 0
	s_add_u32 s2, s2, 0x4000
	s_addc_u32 s3, s3, 0
	s_or_b32 s27, s26, 0x8a0
	s_or_b32 s26, s26, 0xa20
	s_waitcnt vmcnt(24) lgkmcnt(1)
	v_mfma_f32_32x32x16_f16 v[2:17], v[26:29], v[46:49], v[2:17]
	s_waitcnt vmcnt(23)
	v_mfma_f32_32x32x16_f16 v[2:17], v[22:25], v[42:45], v[2:17]
	s_waitcnt vmcnt(22) lgkmcnt(0)
	v_mfma_f32_32x32x16_f16 v[2:17], v[30:33], v[38:41], v[2:17]
	s_waitcnt vmcnt(15)
	v_mfma_f32_32x32x16_f16 v[34:49], v[18:21], v[34:37], 0
	s_nop 9
	v_cvt_pk_f16_f32 v9, v8, v9
	v_cvt_pk_f16_f32 v8, v6, v7
	v_cvt_pk_f16_f32 v7, v4, v5
	v_cvt_pk_f16_f32 v6, v2, v3
	v_cvt_pk_f16_f32 v5, v16, v17
	v_cvt_pk_f16_f32 v4, v14, v15
	v_cvt_pk_f16_f32 v3, v12, v13
	v_mfma_f32_32x32x16_f16 v[34:49], v[26:29], v[54:57], v[34:49]
	v_cvt_pk_f16_f32 v2, v10, v11
	v_mfma_f32_32x32x16_f16 v[34:49], v[22:25], v[50:53], v[34:49]
	s_waitcnt vmcnt(13)
	v_mfma_f32_32x32x16_f16 v[34:49], v[30:33], v[58:61], v[34:49]
	v_mfma_f32_32x32x16_f16 v[18:33], v[6:9], v[126:129], 0
	s_nop 10
	v_cvt_pk_f16_f32 v13, v40, v41
	v_cvt_pk_f16_f32 v12, v38, v39
	v_cvt_pk_f16_f32 v11, v36, v37
	v_cvt_pk_f16_f32 v10, v34, v35
	v_cvt_pk_f16_f32 v17, v48, v49
	v_cvt_pk_f16_f32 v16, v46, v47
	v_cvt_pk_f16_f32 v15, v44, v45
	v_mfma_f32_32x32x16_f16 v[50:65], v[6:9], v[110:113], 0
	v_bitop3_b32 v6, v171, s27, v170 bitop3:0x36
	v_cvt_pk_f16_f32 v14, v42, v43
	v_mfma_f32_32x32x16_f16 v[18:33], v[2:5], v[122:125], v[18:33]
	s_waitcnt vmcnt(12)
	v_mfma_f32_32x32x16_f16 v[50:65], v[2:5], v[106:109], v[50:65]
	ds_read_b128 v[2:5], v6
	ds_read_b128 v[6:9], v6 offset:32768
	v_mfma_f32_32x32x16_f16 v[18:33], v[10:13], v[118:121], v[18:33]
	s_waitcnt vmcnt(11)
	v_mfma_f32_32x32x16_f16 v[50:65], v[10:13], v[94:97], v[50:65]
	s_waitcnt vmcnt(7) lgkmcnt(1)
	v_mfma_f32_32x32x16_f16 v[34:49], v[2:5], v[66:69], 0
	v_mfma_f32_32x32x16_f16 v[18:33], v[14:17], v[114:117], v[18:33]
	v_mfma_f32_32x32x16_f16 v[50:65], v[14:17], v[90:93], v[50:65]
	v_bitop3_b32 v14, v171, s26, v170 bitop3:0x36
	ds_read_b128 v[10:13], v14
	ds_read_b128 v[14:17], v14 offset:32768
	s_nop 7
	v_cvt_pk_f16_f32 v25, v24, v25
	v_cvt_pk_f16_f32 v24, v22, v23
	v_cvt_pk_f16_f32 v23, v20, v21
	v_cvt_pk_f16_f32 v22, v18, v19
	v_cvt_pk_f16_f32 v21, v32, v33
	s_waitcnt vmcnt(6) lgkmcnt(1)
	v_mfma_f32_32x32x16_f16 v[34:49], v[10:13], v[70:73], v[34:49]
	v_cvt_pk_f16_f32 v20, v30, v31
	v_cvt_pk_f16_f32 v19, v28, v29
	v_cvt_pk_f16_f32 v18, v26, v27
	ds_write_b128 v173, v[22:25]
	ds_write_b128 v172, v[18:21]
	v_cvt_pk_f16_f32 v21, v56, v57
	v_cvt_pk_f16_f32 v20, v54, v55
	s_waitcnt vmcnt(5)
	v_mfma_f32_32x32x16_f16 v[34:49], v[6:9], v[74:77], v[34:49]
	v_cvt_pk_f16_f32 v19, v52, v53
	v_cvt_pk_f16_f32 v18, v50, v51
	ds_write_b128 v173, v[18:21] offset:32768
	v_cvt_pk_f16_f32 v21, v64, v65
	v_cvt_pk_f16_f32 v20, v62, v63
	v_cvt_pk_f16_f32 v19, v60, v61
	v_cvt_pk_f16_f32 v18, v58, v59
	s_waitcnt vmcnt(4) lgkmcnt(3)
	v_mfma_f32_32x32x16_f16 v[34:49], v[14:17], v[78:81], v[34:49]
	ds_write_b128 v172, v[18:21] offset:32768
	s_waitcnt vmcnt(3)
	v_mfma_f32_32x32x16_f16 v[66:81], v[2:5], v[82:85], 0
	s_nop 8
	v_cvt_pk_f16_f32 v41, v40, v41
	v_cvt_pk_f16_f32 v40, v38, v39
	v_cvt_pk_f16_f32 v39, v36, v37
	v_cvt_pk_f16_f32 v38, v34, v35
	v_cvt_pk_f16_f32 v85, v48, v49
	v_cvt_pk_f16_f32 v84, v46, v47
	v_cvt_pk_f16_f32 v83, v44, v45
	s_waitcnt vmcnt(2)
	v_mfma_f32_32x32x16_f16 v[66:81], v[10:13], v[86:89], v[66:81]
	v_cvt_pk_f16_f32 v82, v42, v43
	s_waitcnt vmcnt(1)
	v_mfma_f32_32x32x16_f16 v[66:81], v[6:9], v[182:185], v[66:81]
	s_waitcnt vmcnt(0)
	v_mfma_f32_32x32x16_f16 v[66:81], v[14:17], v[186:189], v[66:81]
	v_mfma_f32_32x32x16_f16 v[2:17], v[38:41], v[126:129], 0
	s_nop 10
	v_cvt_pk_f16_f32 v73, v72, v73
	v_cvt_pk_f16_f32 v72, v70, v71
	v_cvt_pk_f16_f32 v70, v66, v67
	v_cvt_pk_f16_f32 v67, v76, v77
	v_cvt_pk_f16_f32 v66, v74, v75
	global_load_dwordx4 v[74:77], v154, s[2:3]
	v_cvt_pk_f16_f32 v71, v68, v69
	v_cvt_pk_f16_f32 v69, v80, v81
	v_cvt_pk_f16_f32 v68, v78, v79
	global_load_dwordx4 v[78:81], v154, s[2:3] offset:1024
	ds_read_b128 v[18:21], v180
	ds_read_b128 v[22:25], v176
	ds_read_b128 v[26:29], v180 offset:32768
	global_load_dwordx4 v[30:33], v154, s[2:3] offset:2048
	v_mfma_f32_32x32x16_f16 v[34:49], v[38:41], v[110:113], 0
	v_mfma_f32_32x32x16_f16 v[2:17], v[82:85], v[122:125], v[2:17]
	v_mfma_f32_32x32x16_f16 v[34:49], v[82:85], v[106:109], v[34:49]
	ds_read_b128 v[82:85], v176 offset:32768
	s_waitcnt vmcnt(2) lgkmcnt(3)
	v_mfma_f32_32x32x16_f16 v[50:65], v[18:21], v[74:77], 0
	v_mfma_f32_32x32x16_f16 v[2:17], v[70:73], v[118:121], v[2:17]
	v_mfma_f32_32x32x16_f16 v[34:49], v[70:73], v[94:97], v[34:49]
	v_lshl_add_u64 v[70:71], s[2:3], 0, v[154:155]
	v_add_co_u32_e32 v152, vcc, s23, v70
	s_nop 1
	v_addc_co_u32_e32 v153, vcc, 0, v71, vcc
	s_waitcnt vmcnt(1) lgkmcnt(2)
	v_mfma_f32_32x32x16_f16 v[50:65], v[22:25], v[78:81], v[50:65]
	v_mfma_f32_32x32x16_f16 v[2:17], v[66:69], v[114:117], v[2:17]
	v_mfma_f32_32x32x16_f16 v[34:49], v[66:69], v[90:93], v[34:49]
	global_load_dwordx4 v[66:69], v154, s[2:3] offset:3072
	s_nop 9
	v_cvt_pk_f16_f32 v9, v8, v9
	v_cvt_pk_f16_f32 v8, v6, v7
	v_cvt_pk_f16_f32 v7, v4, v5
	v_cvt_pk_f16_f32 v6, v2, v3
	v_cvt_pk_f16_f32 v5, v16, v17
	v_cvt_pk_f16_f32 v4, v14, v15
	s_waitcnt vmcnt(1) lgkmcnt(1)
	v_mfma_f32_32x32x16_f16 v[50:65], v[26:29], v[30:33], v[50:65]
	global_load_dwordx4 v[30:33], v168, s[2:3]
	global_load_dwordx4 v[86:89], v[152:153], off offset:1024
	s_nop 0
	global_load_dwordx4 v[168:171], v168, s[0:1]
	v_cvt_pk_f16_f32 v3, v12, v13
	v_cvt_pk_f16_f32 v2, v10, v11
	ds_write_b128 v175, v[6:9]
	ds_write_b128 v174, v[2:5]
	v_cvt_pk_f16_f32 v5, v40, v41
	s_waitcnt vmcnt(3) lgkmcnt(2)
	v_mfma_f32_32x32x16_f16 v[50:65], v[82:85], v[66:69], v[50:65]
	global_load_dwordx4 v[182:185], v154, s[0:1] offset:1024
	v_cvt_pk_f16_f32 v4, v38, v39
	v_cvt_pk_f16_f32 v3, v36, v37
	v_cvt_pk_f16_f32 v2, v34, v35
	ds_write_b128 v175, v[2:5] offset:32768
	v_cvt_pk_f16_f32 v5, v48, v49
	v_cvt_pk_f16_f32 v4, v46, v47
	s_waitcnt vmcnt(3)
	v_mfma_f32_32x32x16_f16 v[66:81], v[18:21], v[30:33], 0
	global_load_dwordx4 v[18:21], v[152:153], off offset:2048
	v_cvt_pk_f16_f32 v3, v44, v45
	v_cvt_pk_f16_f32 v2, v42, v43
	ds_write_b128 v174, v[2:5] offset:32768
	v_cvt_pk_f16_f32 v57, v56, v57
	v_cvt_pk_f16_f32 v56, v54, v55
	v_cvt_pk_f16_f32 v55, v52, v53
	s_waitcnt vmcnt(3)
	v_mfma_f32_32x32x16_f16 v[66:81], v[22:25], v[86:89], v[66:81]
	global_load_dwordx4 v[22:25], v[152:153], off offset:3072
	v_cvt_pk_f16_f32 v54, v50, v51
	s_waitcnt vmcnt(1)
	v_mfma_f32_32x32x16_f16 v[66:81], v[26:29], v[18:21], v[66:81]
	v_lshl_add_u64 v[18:19], s[0:1], 0, v[154:155]
	v_add_co_u32_e32 v152, vcc, s23, v18
	s_nop 1
	v_addc_co_u32_e32 v153, vcc, 0, v19, vcc
	global_load_dwordx4 v[86:89], v[152:153], off offset:1024
	s_waitcnt vmcnt(1)
	v_mfma_f32_32x32x16_f16 v[66:81], v[82:85], v[22:25], v[66:81]
	v_cvt_pk_f16_f32 v85, v64, v65
	v_cvt_pk_f16_f32 v84, v62, v63
	v_cvt_pk_f16_f32 v83, v60, v61
	v_cvt_pk_f16_f32 v82, v58, v59
	v_mfma_f32_32x32x16_f16 v[18:33], v[54:57], v[126:129], 0
	s_nop 6
	v_cvt_pk_f16_f32 v73, v72, v73
	v_cvt_pk_f16_f32 v72, v70, v71
	v_cvt_pk_f16_f32 v70, v66, v67
	v_cvt_pk_f16_f32 v67, v76, v77
	v_cvt_pk_f16_f32 v66, v74, v75
	global_load_dwordx4 v[74:77], v154, s[0:1]
	ds_read_b128 v[2:5], v181
	ds_read_b128 v[6:9], v177
	ds_read_b128 v[10:13], v181 offset:32768
	global_load_dwordx4 v[14:17], v154, s[0:1] offset:2048
	global_load_dwordx4 v[34:37], v154, s[0:1] offset:3072
	v_mfma_f32_32x32x16_f16 v[50:65], v[54:57], v[110:113], 0
	v_cvt_pk_f16_f32 v71, v68, v69
	v_cvt_pk_f16_f32 v69, v80, v81
	v_cvt_pk_f16_f32 v68, v78, v79
	v_mfma_f32_32x32x16_f16 v[18:33], v[82:85], v[122:125], v[18:33]
	v_mfma_f32_32x32x16_f16 v[50:65], v[82:85], v[106:109], v[50:65]
	ds_read_b128 v[82:85], v177 offset:32768
	v_mfma_f32_32x32x16_f16 v[18:33], v[70:73], v[118:121], v[18:33]
	v_mfma_f32_32x32x16_f16 v[50:65], v[70:73], v[94:97], v[50:65]
	v_mfma_f32_32x32x16_f16 v[18:33], v[66:69], v[114:117], v[18:33]
	v_mfma_f32_32x32x16_f16 v[50:65], v[66:69], v[90:93], v[50:65]
	s_nop 10
	v_cvt_pk_f16_f32 v25, v24, v25
	v_cvt_pk_f16_f32 v24, v22, v23
	v_cvt_pk_f16_f32 v23, v20, v21
	v_cvt_pk_f16_f32 v22, v18, v19
	ds_write_b128 v132, v[22:25]
	s_waitcnt vmcnt(2) lgkmcnt(4)
	v_mfma_f32_32x32x16_f16 v[66:81], v[2:5], v[74:77], 0
	s_waitcnt lgkmcnt(3)
	v_mfma_f32_32x32x16_f16 v[66:81], v[6:9], v[182:185], v[66:81]
	s_waitcnt vmcnt(1) lgkmcnt(2)
	v_mfma_f32_32x32x16_f16 v[66:81], v[10:13], v[14:17], v[66:81]
	s_waitcnt vmcnt(0) lgkmcnt(1)
	v_mfma_f32_32x32x16_f16 v[66:81], v[82:85], v[34:37], v[66:81]
	v_mfma_f32_32x32x16_f16 v[34:49], v[2:5], v[168:171], 0
	global_load_dwordx4 v[2:5], v[152:153], off offset:2048
	s_nop 9
	v_cvt_pk_f16_f32 v73, v72, v73
	v_cvt_pk_f16_f32 v72, v70, v71
	v_cvt_pk_f16_f32 v71, v68, v69
	v_cvt_pk_f16_f32 v70, v66, v67
	v_cvt_pk_f16_f32 v69, v80, v81
	v_cvt_pk_f16_f32 v68, v78, v79
	v_mfma_f32_32x32x16_f16 v[34:49], v[6:9], v[86:89], v[34:49]
	global_load_dwordx4 v[6:9], v[152:153], off offset:3072
	v_cvt_pk_f16_f32 v67, v76, v77
	v_cvt_pk_f16_f32 v66, v74, v75
	s_waitcnt vmcnt(1)
	v_mfma_f32_32x32x16_f16 v[34:49], v[10:13], v[2:5], v[34:49]
	s_waitcnt vmcnt(0)
	v_mfma_f32_32x32x16_f16 v[34:49], v[82:85], v[6:9], v[34:49]
	v_mfma_f32_32x32x16_f16 v[2:17], v[70:73], v[126:129], 0
	s_nop 10
	v_cvt_pk_f16_f32 v41, v40, v41
	v_cvt_pk_f16_f32 v40, v38, v39
	v_cvt_pk_f16_f32 v38, v34, v35
	v_cvt_pk_f16_f32 v35, v44, v45
	v_cvt_pk_f16_f32 v34, v42, v43
	v_cvt_pk_f16_f32 v45, v32, v33
	v_cvt_pk_f16_f32 v44, v30, v31
	v_cvt_pk_f16_f32 v43, v28, v29
	v_cvt_pk_f16_f32 v42, v26, v27
	v_mfma_f32_32x32x16_f16 v[18:33], v[70:73], v[110:113], 0
	v_cvt_pk_f16_f32 v39, v36, v37
	v_cvt_pk_f16_f32 v37, v48, v49
	v_cvt_pk_f16_f32 v36, v46, v47
	ds_write_b128 v131, v[42:45]
	v_cvt_pk_f16_f32 v45, v56, v57
	v_cvt_pk_f16_f32 v44, v54, v55
	v_cvt_pk_f16_f32 v43, v52, v53
	v_mfma_f32_32x32x16_f16 v[2:17], v[66:69], v[122:125], v[2:17]
	v_cvt_pk_f16_f32 v42, v50, v51
	ds_write_b128 v132, v[42:45] offset:32768
	v_cvt_pk_f16_f32 v45, v64, v65
	v_cvt_pk_f16_f32 v44, v62, v63
	v_cvt_pk_f16_f32 v43, v60, v61
	v_cvt_pk_f16_f32 v42, v58, v59
	ds_write_b128 v131, v[42:45] offset:32768
	v_mfma_f32_32x32x16_f16 v[18:33], v[66:69], v[106:109], v[18:33]
	v_mfma_f32_32x32x16_f16 v[2:17], v[38:41], v[118:121], v[2:17]
	v_mfma_f32_32x32x16_f16 v[18:33], v[38:41], v[94:97], v[18:33]
	v_mfma_f32_32x32x16_f16 v[2:17], v[34:37], v[114:117], v[2:17]
	v_mfma_f32_32x32x16_f16 v[18:33], v[34:37], v[90:93], v[18:33]
	s_nop 10
	v_cvt_pk_f16_f32 v9, v8, v9
	v_cvt_pk_f16_f32 v8, v6, v7
	v_cvt_pk_f16_f32 v7, v4, v5
	v_cvt_pk_f16_f32 v6, v2, v3
	v_cvt_pk_f16_f32 v5, v16, v17
	v_cvt_pk_f16_f32 v4, v14, v15
	v_cvt_pk_f16_f32 v3, v12, v13
	v_cvt_pk_f16_f32 v2, v10, v11
	ds_write_b128 v135, v[6:9]
	ds_write_b128 v133, v[2:5]
	v_cvt_pk_f16_f32 v5, v24, v25
	v_cvt_pk_f16_f32 v4, v22, v23
	v_cvt_pk_f16_f32 v3, v20, v21
	v_cvt_pk_f16_f32 v2, v18, v19
	ds_write_b128 v135, v[2:5] offset:32768
	v_cvt_pk_f16_f32 v5, v32, v33
	v_cvt_pk_f16_f32 v4, v30, v31
	v_cvt_pk_f16_f32 v3, v28, v29
	v_cvt_pk_f16_f32 v2, v26, v27
	ds_write_b128 v133, v[2:5] offset:32768
	s_setprio 0
	s_waitcnt lgkmcnt(0)
	s_barrier
	s_cmp_lt_i32 s22, 0
	s_cbranch_scc0 .Lno_pref
	s_add_u32 s36, s10, 0x140000
	s_addc_u32 s37, s11, 0
	v_lshlrev_b32_e32 v192, 3, v156
	v_lshlrev_b32_e32 v193, 3, v167
	global_load_dwordx2 v[190:191], v192, s[36:37]
	global_load_dwordx2 v[194:195], v193, s[36:37] offset:2048
